# speedup vs baseline: 1.0240x; 1.0114x over previous
.Lk2_needref:
	s_cmp_lg_u32 s58, 0
	s_cselect_b32 s48, -1, 0
	s_cmp_lg_u32 s60, 0
	s_cselect_b32 s49, -1, 0
	s_mov_b64 exec, s[48:49]
	v_and_b32_e32 v29, 31, v1
	v_lshlrev_b32_e32 v30, 2, v29
	v_lshlrev_b32_e32 v29, 3, v29
	v_mov_b32_e32 v31, 1
	s_mov_b32 s3, 4
.Lk2_nr_loop:
	ds_read_b64 v[116:117], v29 offset:0
	ds_read_b64 v[118:119], v29 offset:256
	ds_read_b64 v[120:121], v29 offset:512
	ds_read_b64 v[122:123], v29 offset:768
	s_waitcnt lgkmcnt(0)
	v_add_f64 v[116:117], v[116:117], -v[64:65]
	v_add_f64 v[118:119], v[118:119], -v[64:65]
	v_add_f64 v[120:121], v[120:121], -v[64:65]
	v_add_f64 v[122:123], v[122:123], -v[64:65]
	v_cmp_ge_f64_e64 s[50:51], s[32:33], |v[116:117]|
	s_and_saveexec_b64 s[46:47], s[50:51]
	ds_write_b32 v30, v31 offset:8448
	s_mov_b64 exec, s[46:47]
	v_cmp_ge_f64_e64 s[50:51], s[32:33], |v[118:119]|
	s_and_saveexec_b64 s[46:47], s[50:51]
	ds_write_b32 v30, v31 offset:8576
	s_mov_b64 exec, s[46:47]
	v_cmp_ge_f64_e64 s[50:51], s[32:33], |v[120:121]|
	s_and_saveexec_b64 s[46:47], s[50:51]
	ds_write_b32 v30, v31 offset:8704
	s_mov_b64 exec, s[46:47]
	v_cmp_ge_f64_e64 s[50:51], s[32:33], |v[122:123]|
	s_and_saveexec_b64 s[46:47], s[50:51]
	ds_write_b32 v30, v31 offset:8832
	s_mov_b64 exec, s[46:47]
	v_add_u32_e32 v29, 0x400, v29
	v_add_u32_e32 v30, 0x200, v30
	s_sub_u32 s3, s3, 1
	s_cmp_lg_u32 s3, 0
	s_cbranch_scc1 .Lk2_nr_loop
	s_mov_b64 exec, -1
	ds_write_b32 v105, v31 offset:16
	s_waitcnt lgkmcnt(0)
	s_branch .Lk2_b3

.Lk2_rf_done:
	s_waitcnt lgkmcnt(0)
	s_barrier
	s_cmp_eq_u32 s61, 0
	s_cbranch_scc1 .Lk2_dst_stores
	v_lshrrev_b32_e32 v29, 5, v1
	v_lshl_add_u32 v29, s25, 3, v29
	v_lshlrev_b32_e32 v30, 3, v29
	ds_read_b64 v[64:65], v30 offset:0
	v_and_b32_e32 v31, 31, v1
	v_lshlrev_b32_e32 v30, 3, v31
	v_mov_b32_e32 v66, 0
	s_mov_b32 s3, 4
.Lk2_rc_loop:
	ds_read_b64 v[116:117], v30 offset:0
	ds_read_b64 v[118:119], v30 offset:256
	ds_read_b64 v[120:121], v30 offset:512
	ds_read_b64 v[122:123], v30 offset:768
	s_waitcnt lgkmcnt(0)
	v_cmp_gt_f64_e32 vcc, v[116:117], v[64:65]
	v_cmp_eq_f64_e64 s[48:49], v[116:117], v[64:65]
	v_cmp_lt_u32_e64 s[50:51], v31, v29
	s_and_b64 s[48:49], s[48:49], s[50:51]
	s_or_b64 s[48:49], s[48:49], vcc
	v_addc_co_u32_e64 v66, s[50:51], 0, v66, s[48:49]
	v_add_u32_e32 v28, 32, v31
	v_cmp_gt_f64_e32 vcc, v[118:119], v[64:65]
	v_cmp_eq_f64_e64 s[48:49], v[118:119], v[64:65]
	v_cmp_lt_u32_e64 s[50:51], v28, v29
	s_and_b64 s[48:49], s[48:49], s[50:51]
	s_or_b64 s[48:49], s[48:49], vcc
	v_addc_co_u32_e64 v66, s[50:51], 0, v66, s[48:49]
	v_add_u32_e32 v28, 64, v31
	v_cmp_gt_f64_e32 vcc, v[120:121], v[64:65]
	v_cmp_eq_f64_e64 s[48:49], v[120:121], v[64:65]
	v_cmp_lt_u32_e64 s[50:51], v28, v29
	s_and_b64 s[48:49], s[48:49], s[50:51]
	s_or_b64 s[48:49], s[48:49], vcc
	v_addc_co_u32_e64 v66, s[50:51], 0, v66, s[48:49]
	v_add_u32_e32 v28, 96, v31
	v_cmp_gt_f64_e32 vcc, v[122:123], v[64:65]
	v_cmp_eq_f64_e64 s[48:49], v[122:123], v[64:65]
	v_cmp_lt_u32_e64 s[50:51], v28, v29
	s_and_b64 s[48:49], s[48:49], s[50:51]
	s_or_b64 s[48:49], s[48:49], vcc
	v_addc_co_u32_e64 v66, s[50:51], 0, v66, s[48:49]
	v_add_u32_e32 v30, 0x400, v30
	v_add_u32_e32 v31, 0x80, v31
	s_sub_u32 s3, s3, 1
	s_cmp_lg_u32 s3, 0
	s_cbranch_scc1 .Lk2_rc_loop
	s_nop 1
	v_add_u32_dpp v66, v66, v66 quad_perm:[1,0,3,2] row_mask:0xf bank_mask:0xf
	s_nop 1
	v_add_u32_dpp v66, v66, v66 quad_perm:[2,3,0,1] row_mask:0xf bank_mask:0xf
	s_nop 1
	v_add_u32_dpp v66, v66, v66 row_half_mirror row_mask:0xf bank_mask:0xf
	s_nop 1
	v_add_u32_dpp v66, v66, v66 row_mirror row_mask:0xf bank_mask:0xf
	s_nop 1
	v_add_u32_dpp v66, v66, v66 row_bcast:15 row_mask:0xa bank_mask:0xf
	s_nop 1
	v_readlane_b32 s52, v66, 31
	v_readlane_b32 s53, v66, 63
	s_cmp_lg_u32 s58, 0
	s_cselect_b32 s54, s52, s54
	s_cmp_lg_u32 s60, 0
	s_cselect_b32 s56, s53, s56
	s_waitcnt vmcnt(0)
	s_branch .Lk2_dst_stores
